# early combine pass throttled with s_sleep between rows so it does not compete with the tail GEMM units for HBM
# baseline (speedup 1.0000x reference)
; __device__ __forceinline__ float bf_lo(unsigned w) { return __uint_as_float(w << 16); }
; __device__ __forceinline__ float bf_hi(unsigned w) { return __uint_as_float(w & 0xffff0000u); }
; __device__ __forceinline__ f32x4 ld4_bf(const bf16_t* p) { const u32x2 w = *(const u32x2*)p; return (f32x4){bf_lo(w.x), bf_hi(w.x), bf_lo(w.y), bf_hi(w.y)}; }
; __device__ __forceinline__ float sq4(const f32x4 v) { return (v[0] * v[0] + v[1] * v[1]) + (v[2] * v[2] + v[3] * v[3]); }
; __device__ __forceinline__ void phase_final(const Ctx& P, volatile LAS int* tab, int vcu, int G) {
;     ...
;     for (int row = gw; row < ML; row += NGW) {
;         const int e1 = tok[row * 8], pos1 = tok[row * 8 + 1], e2 = tok[row * 8 + 2], pos2 = tok[row * 8 + 3]; const float p1 = ((const float*)tok)[row * 8 + 4], p2 = ((const float*)tok)[row * 8 + 5];
;         const bf16_t* y1 = YB + (size_t)(tab[8 + e1] * 256 + pos1) * DM; const bf16_t* y2 = YB + (size_t)(tab[8 + e2] * 256 + pos2) * DM;
;         const bf16_t* xr = (const bf16_t*)(P.ws + WS_XA) + (size_t)row * DM; const float* g2 = mod + (size_t)(row >> 12) * NMOD + 5 * DM;
;         f32x4 v[8]; float ss = 0.f;
; #pragma unroll
;         for (int j = 0; j < 8; ++j) { const int c = 4 * lane + 256 * j; const f32x4 x4 = ld4_bf(xr + c), g4 = *(const f32x4*)(g2 + c); const u32x2 a = *(const u32x2*)(y1 + c), b = *(const u32x2*)(y2 + c);
;             const f32x4 ya = (f32x4){bf_lo(a.x), bf_hi(a.x), bf_lo(a.y), bf_hi(a.y)}, yb = (f32x4){bf_lo(b.x), bf_hi(b.x), bf_lo(b.y), bf_hi(b.y)};
;             v[j] = x4 + g4 * (ya * p1 + yb * p2); ss += sq4(v[j]); }
.LBB0_2712:
	v_mov_b32_e32 v16, v194
	v_mov_b32_e32 v17, v195
	v_mov_b32_e32 v18, v196
	v_mov_b32_e32 v19, v197
	v_mov_b32_e32 v46, v198
	v_mov_b32_e32 v47, v199
	v_max_i32_e32 v200, v194, v196
	s_ashr_i32 s3, s10, 12
	s_mul_hi_i32 s8, s3, 0xc000
	s_mul_i32 s3, s3, 0xc000
	s_add_u32 s3, s36, s3
	s_addc_u32 s9, s37, s8
	s_add_u32 s8, s3, 0x146000
	s_addc_u32 s9, s9, 0
	s_add_i32 s10, s10, s0
	s_add_i32 s2, s2, s13
	s_ashr_i32 s3, s2, 31
	s_lshl_b64 s[14:15], s[2:3], 2
	s_add_u32 s14, s11, s14
	s_addc_u32 s15, s12, s15
	s_cmpk_lt_i32 s10, 0x4000
	s_cselect_b32 s17, 1, 0
	v_readfirstlane_b32 s16, v200
	s_cmp_lt_i32 s16, s20
	s_cbranch_scc1 .Lp16_skip
	s_cmp_ge_i32 s16, s21
	s_cbranch_scc1 .Lp16_skip
	v_lshlrev_b32_e32 v0, 2, v16
	v_lshlrev_b32_e32 v1, 2, v18
	v_add_u32_e32 v0, s1, v0
	v_add_u32_e32 v1, s1, v1
	ds_read_b32 v16, v0 offset:32
	ds_read_b32 v18, v1 offset:32
	global_load_dwordx2 v[48:49], v[34:35], off offset:-2048
	global_load_dwordx2 v[50:51], v[34:35], off offset:-1536
	global_load_dwordx2 v[52:53], v[34:35], off offset:-1024
	global_load_dwordx4 v[0:3], v28, s[8:9]
	global_load_dwordx2 v[54:55], v[34:35], off offset:-512
	global_load_dwordx4 v[8:11], v64, s[8:9]
	global_load_dwordx4 v[4:7], v65, s[8:9]
	global_load_dwordx4 v[12:15], v66, s[8:9]
	global_load_dwordx2 v[56:57], v[34:35], off
	global_load_dwordx4 v[20:23], v36, s[8:9]
	global_load_dwordx4 v[24:27], v38, s[8:9]
	global_load_dwordx2 v[76:77], v[34:35], off offset:512
	global_load_dwordx2 v[78:79], v[34:35], off offset:1024
	global_load_dwordx2 v[80:81], v[34:35], off offset:1536
	global_load_dwordx4 v[68:71], v40, s[8:9]
	global_load_dwordx4 v[72:75], v42, s[8:9]
	v_lshl_add_u64 v[34:35], v[34:35], 0, s[6:7]
	s_waitcnt lgkmcnt(0)
	v_lshlrev_b32_e32 v16, 8, v16
	v_lshlrev_b32_e32 v18, 8, v18
	v_add_u32_e32 v16, v16, v17
	v_add_u32_e32 v18, v18, v19
	v_ashrrev_i32_e32 v17, 31, v16
	v_ashrrev_i32_e32 v19, 31, v18
	v_lshlrev_b64 v[16:17], 12, v[16:17]
	v_lshlrev_b64 v[18:19], 12, v[18:19]
	v_lshl_add_u64 v[16:17], v[30:31], 0, v[16:17]
	v_lshl_add_u64 v[18:19], v[30:31], 0, v[18:19]
	global_load_dwordx2 v[84:85], v[16:17], off
	global_load_dwordx2 v[86:87], v[18:19], off
	global_load_dwordx2 v[88:89], v[16:17], off offset:512
	global_load_dwordx2 v[90:91], v[18:19], off offset:512
	global_load_dwordx2 v[92:93], v[16:17], off offset:1024
	global_load_dwordx2 v[94:95], v[18:19], off offset:1024
	global_load_dwordx2 v[96:97], v[16:17], off offset:1536
	global_load_dwordx2 v[98:99], v[18:19], off offset:1536
	global_load_dwordx2 v[100:101], v[16:17], off offset:2048
	global_load_dwordx2 v[102:103], v[18:19], off offset:2048
	global_load_dwordx2 v[104:105], v[16:17], off offset:2560
	global_load_dwordx2 v[106:107], v[16:17], off offset:3072
	global_load_dwordx2 v[108:109], v[16:17], off offset:3584
	global_load_dwordx2 v[110:111], v[18:19], off offset:2560
	global_load_dwordx2 v[112:113], v[18:19], off offset:3072
	global_load_dwordx2 v[114:115], v[18:19], off offset:3584
	global_load_dwordx4 v[194:197], v29, s[14:15]
	global_load_dwordx2 v[198:199], v29, s[14:15] offset:16
	s_waitcnt vmcnt(2)
	v_lshlrev_b32_e32 v116, 16, v48
	v_and_b32_e32 v117, 0xffff0000, v48
	v_lshlrev_b32_e32 v48, 16, v49
	v_and_b32_e32 v49, 0xffff0000, v49
	v_lshlrev_b32_e32 v118, 16, v50
	v_and_b32_e32 v119, 0xffff0000, v50
	v_lshlrev_b32_e32 v50, 16, v51
	v_and_b32_e32 v51, 0xffff0000, v51
	v_lshlrev_b32_e32 v120, 16, v52
	v_and_b32_e32 v121, 0xffff0000, v52
	v_lshlrev_b32_e32 v52, 16, v53
	v_and_b32_e32 v53, 0xffff0000, v53
	v_lshlrev_b32_e32 v124, 16, v56
	v_and_b32_e32 v125, 0xffff0000, v56
	v_lshlrev_b32_e32 v132, 16, v86
	v_and_b32_e32 v133, 0xffff0000, v86
	v_lshlrev_b32_e32 v86, 16, v87
	v_and_b32_e32 v87, 0xffff0000, v87
	v_lshlrev_b32_e32 v136, 16, v90
	v_and_b32_e32 v137, 0xffff0000, v90
	v_lshlrev_b32_e32 v90, 16, v91
	v_and_b32_e32 v91, 0xffff0000, v91
	v_lshlrev_b32_e32 v82, 16, v84
	v_and_b32_e32 v83, 0xffff0000, v84
	v_lshlrev_b32_e32 v84, 16, v85
	v_and_b32_e32 v85, 0xffff0000, v85
	v_lshlrev_b32_e32 v134, 16, v88
	v_and_b32_e32 v135, 0xffff0000, v88
	v_lshlrev_b32_e32 v88, 16, v89
	v_and_b32_e32 v89, 0xffff0000, v89
	v_lshlrev_b32_e32 v140, 16, v94
	v_and_b32_e32 v141, 0xffff0000, v94
	v_lshlrev_b32_e32 v94, 16, v95
	v_and_b32_e32 v95, 0xffff0000, v95
	v_lshlrev_b32_e32 v148, 16, v102
	v_and_b32_e32 v149, 0xffff0000, v102
	v_lshlrev_b32_e32 v102, 16, v103
	v_and_b32_e32 v103, 0xffff0000, v103
	v_lshlrev_b32_e32 v156, 16, v112
	v_and_b32_e32 v157, 0xffff0000, v112
	v_lshlrev_b32_e32 v112, 16, v113
	v_and_b32_e32 v113, 0xffff0000, v113
	v_pk_mul_f32 v[86:87], v[46:47], v[86:87] op_sel:[1,0]
	v_pk_mul_f32 v[132:133], v[46:47], v[132:133] op_sel:[1,0]
	v_pk_mul_f32 v[90:91], v[46:47], v[90:91] op_sel:[1,0]
	v_pk_mul_f32 v[136:137], v[46:47], v[136:137] op_sel:[1,0]
	v_lshlrev_b32_e32 v138, 16, v92
	v_and_b32_e32 v139, 0xffff0000, v92
	v_lshlrev_b32_e32 v92, 16, v93
	v_and_b32_e32 v93, 0xffff0000, v93
	v_lshlrev_b32_e32 v144, 16, v98
	v_and_b32_e32 v145, 0xffff0000, v98
	v_lshlrev_b32_e32 v98, 16, v99
	v_and_b32_e32 v99, 0xffff0000, v99
	v_lshlrev_b32_e32 v146, 16, v100
	v_and_b32_e32 v147, 0xffff0000, v100
	v_lshlrev_b32_e32 v100, 16, v101
	v_and_b32_e32 v101, 0xffff0000, v101
	v_lshlrev_b32_e32 v152, 16, v110
	v_and_b32_e32 v153, 0xffff0000, v110
	v_lshlrev_b32_e32 v110, 16, v111
	v_and_b32_e32 v111, 0xffff0000, v111
	v_lshlrev_b32_e32 v154, 16, v106
	v_and_b32_e32 v155, 0xffff0000, v106
	v_lshlrev_b32_e32 v106, 16, v107
	v_and_b32_e32 v107, 0xffff0000, v107
	v_lshlrev_b32_e32 v160, 16, v114
	v_and_b32_e32 v161, 0xffff0000, v114
	v_lshlrev_b32_e32 v114, 16, v115
; __device__ __forceinline__ float bf_lo(unsigned w) { return __uint_as_float(w << 16); }
; __device__ __forceinline__ float bf_hi(unsigned w) { return __uint_as_float(w & 0xffff0000u); }
; __device__ __forceinline__ f32x4 ld4_bf(const bf16_t* p) { const u32x2 w = *(const u32x2*)p; return (f32x4){bf_lo(w.x), bf_hi(w.x), bf_lo(w.y), bf_hi(w.y)}; }
; __device__ __forceinline__ float sq4(const f32x4 v) { return (v[0] * v[0] + v[1] * v[1]) + (v[2] * v[2] + v[3] * v[3]); }
; __device__ __forceinline__ void phase_final(const Ctx& P, volatile LAS int* tab, int vcu, int G) {
;     ...
;         for (int j = 0; j < 8; ++j) { const int c = 4 * lane + 256 * j; const f32x4 x4 = ld4_bf(xr + c), g4 = *(const f32x4*)(g2 + c); const u32x2 a = *(const u32x2*)(y1 + c), b = *(const u32x2*)(y2 + c);
;             const f32x4 ya = (f32x4){bf_lo(a.x), bf_hi(a.x), bf_lo(a.y), bf_hi(a.y)}, yb = (f32x4){bf_lo(b.x), bf_hi(b.x), bf_lo(b.y), bf_hi(b.y)};
;             v[j] = x4 + g4 * (ya * p1 + yb * p2); ss += sq4(v[j]); }
;         ss = wave_sum(ss); const float rstd = __builtin_amdgcn_rsqf(ss * (1.0f / DM) + EPS);
	v_and_b32_e32 v115, 0xffff0000, v115
	v_pk_mul_f32 v[140:141], v[46:47], v[140:141] op_sel:[1,0]
	v_pk_mul_f32 v[94:95], v[46:47], v[94:95] op_sel:[1,0]
	v_pk_mul_f32 v[102:103], v[46:47], v[102:103] op_sel:[1,0]
	v_pk_mul_f32 v[112:113], v[46:47], v[112:113] op_sel:[1,0]
	v_pk_fma_f32 v[82:83], v[46:47], v[82:83], v[132:133] op_sel_hi:[0,1,1]
	v_pk_fma_f32 v[84:85], v[46:47], v[84:85], v[86:87] op_sel_hi:[0,1,1]
	v_pk_fma_f32 v[86:87], v[46:47], v[134:135], v[136:137] op_sel_hi:[0,1,1]
	v_pk_fma_f32 v[88:89], v[46:47], v[88:89], v[90:91] op_sel_hi:[0,1,1]
	v_lshlrev_b32_e32 v56, 16, v57
	v_and_b32_e32 v57, 0xffff0000, v57
	v_lshlrev_b32_e32 v128, 16, v78
	v_and_b32_e32 v129, 0xffff0000, v78
	v_lshlrev_b32_e32 v78, 16, v79
	v_and_b32_e32 v79, 0xffff0000, v79
	v_lshlrev_b32_e32 v142, 16, v96
	v_and_b32_e32 v143, 0xffff0000, v96
	v_lshlrev_b32_e32 v96, 16, v97
	v_and_b32_e32 v97, 0xffff0000, v97
	v_lshlrev_b32_e32 v150, 16, v104
	v_and_b32_e32 v151, 0xffff0000, v104
	v_lshlrev_b32_e32 v104, 16, v105
	v_and_b32_e32 v105, 0xffff0000, v105
	v_lshlrev_b32_e32 v158, 16, v108
	v_and_b32_e32 v159, 0xffff0000, v108
	v_lshlrev_b32_e32 v108, 16, v109
	v_and_b32_e32 v109, 0xffff0000, v109
	v_pk_mul_f32 v[98:99], v[46:47], v[98:99] op_sel:[1,0]
	v_pk_mul_f32 v[144:145], v[46:47], v[144:145] op_sel:[1,0]
	v_pk_mul_f32 v[148:149], v[46:47], v[148:149] op_sel:[1,0]
	v_pk_mul_f32 v[152:153], v[46:47], v[152:153] op_sel:[1,0]
	v_pk_mul_f32 v[110:111], v[46:47], v[110:111] op_sel:[1,0]
	v_pk_mul_f32 v[156:157], v[46:47], v[156:157] op_sel:[1,0]
	v_pk_mul_f32 v[114:115], v[46:47], v[114:115] op_sel:[1,0]
	v_pk_mul_f32 v[160:161], v[46:47], v[160:161] op_sel:[1,0]
	v_pk_fma_f32 v[90:91], v[46:47], v[92:93], v[94:95] op_sel_hi:[0,1,1]
	v_pk_fma_f32 v[92:93], v[46:47], v[138:139], v[140:141] op_sel_hi:[0,1,1]
	v_pk_fma_f32 v[100:101], v[46:47], v[100:101], v[102:103] op_sel_hi:[0,1,1]
	v_pk_fma_f32 v[106:107], v[46:47], v[106:107], v[112:113] op_sel_hi:[0,1,1]
	v_pk_fma_f32 v[2:3], v[2:3], v[84:85], v[48:49]
	v_pk_fma_f32 v[0:1], v[0:1], v[82:83], v[116:117]
	v_pk_fma_f32 v[10:11], v[10:11], v[88:89], v[50:51]
	v_pk_fma_f32 v[8:9], v[8:9], v[86:87], v[118:119]
	v_lshlrev_b32_e32 v122, 16, v54
	v_and_b32_e32 v123, 0xffff0000, v54
	v_lshlrev_b32_e32 v54, 16, v55
	v_and_b32_e32 v55, 0xffff0000, v55
	v_lshlrev_b32_e32 v130, 16, v80
	v_and_b32_e32 v131, 0xffff0000, v80
	v_lshlrev_b32_e32 v80, 16, v81
	v_and_b32_e32 v81, 0xffff0000, v81
	v_pk_fma_f32 v[94:95], v[46:47], v[142:143], v[144:145] op_sel_hi:[0,1,1]
	v_pk_fma_f32 v[96:97], v[46:47], v[96:97], v[98:99] op_sel_hi:[0,1,1]
	v_pk_fma_f32 v[98:99], v[46:47], v[146:147], v[148:149] op_sel_hi:[0,1,1]
	v_pk_fma_f32 v[102:103], v[46:47], v[104:105], v[110:111] op_sel_hi:[0,1,1]
	v_pk_fma_f32 v[104:105], v[46:47], v[150:151], v[152:153] op_sel_hi:[0,1,1]
	v_pk_fma_f32 v[110:111], v[46:47], v[154:155], v[156:157] op_sel_hi:[0,1,1]
	v_pk_fma_f32 v[112:113], v[46:47], v[158:159], v[160:161] op_sel_hi:[0,1,1]
	v_pk_fma_f32 v[46:47], v[46:47], v[108:109], v[114:115] op_sel_hi:[0,1,1]
	v_pk_fma_f32 v[4:5], v[4:5], v[92:93], v[120:121]
	v_pk_fma_f32 v[6:7], v[6:7], v[90:91], v[52:53]
	v_pk_fma_f32 v[22:23], v[22:23], v[100:101], v[56:57]
	v_pk_fma_f32 v[48:49], v[70:71], v[106:107], v[78:79]
	v_mov_b32_e32 v56, v1
	v_mov_b32_e32 v57, v9
	v_mov_b32_e32 v70, v3
	v_mov_b32_e32 v71, v11
	v_pk_fma_f32 v[14:15], v[14:15], v[96:97], v[54:55]
	v_pk_fma_f32 v[50:51], v[68:69], v[110:111], v[128:129]
	v_pk_fma_f32 v[46:47], v[74:75], v[46:47], v[80:81]
	v_pk_fma_f32 v[52:53], v[72:73], v[112:113], v[130:131]
	v_mov_b32_e32 v54, v0
	v_mov_b32_e32 v55, v8
	v_mov_b32_e32 v68, v2
	v_mov_b32_e32 v69, v10
	v_pk_mul_f32 v[72:73], v[6:7], v[6:7]
	v_pk_mul_f32 v[74:75], v[4:5], v[4:5]
	v_pk_mul_f32 v[56:57], v[56:57], v[56:57]
	v_pk_mul_f32 v[70:71], v[70:71], v[70:71]
	v_lshlrev_b32_e32 v126, 16, v76
	v_and_b32_e32 v127, 0xffff0000, v76
	v_lshlrev_b32_e32 v76, 16, v77
	v_and_b32_e32 v77, 0xffff0000, v77
	v_pk_fma_f32 v[12:13], v[12:13], v[94:95], v[122:123]
	v_pk_mov_b32 v[88:89], v[74:75], v[72:73] op_sel:[1,0]
	v_mov_b32_e32 v75, v73
	v_pk_fma_f32 v[54:55], v[54:55], v[54:55], v[56:57]
	v_pk_fma_f32 v[56:57], v[68:69], v[68:69], v[70:71]
	v_pk_fma_f32 v[20:21], v[20:21], v[98:99], v[124:125]
	v_pk_fma_f32 v[26:27], v[26:27], v[102:103], v[76:77]
	v_mul_f32_e32 v76, v13, v13
	v_mul_f32_e32 v78, v15, v15
	v_pk_add_f32 v[68:69], v[88:89], v[74:75]
	v_pk_add_f32 v[54:55], v[54:55], v[56:57]
	v_pk_fma_f32 v[24:25], v[24:25], v[104:105], v[126:127]
	v_mul_f32_e32 v87, v20, v20
	v_mul_f32_e32 v90, v21, v21
	v_mul_f32_e32 v91, v22, v22
	v_mul_f32_e32 v92, v23, v23
	v_pk_fma_f32 v[72:73], v[12:13], v[12:13], v[76:77] op_sel_hi:[1,1,0]
	v_pk_fma_f32 v[76:77], v[14:15], v[14:15], v[78:79] op_sel_hi:[1,1,0]
	v_pk_add_f32 v[56:57], v[68:69], v[68:69] op_sel:[0,1] op_sel_hi:[1,0]
	v_pk_add_f32 v[54:55], v[54:55], v[54:55] op_sel:[0,1] op_sel_hi:[1,0]
	v_pk_mul_f32 v[80:81], v[26:27], v[26:27]
	v_pk_mul_f32 v[82:83], v[24:25], v[24:25]
	v_mov_b32_e32 v73, v91
	v_mov_b32_e32 v77, v92
	v_mov_b32_e32 v57, v90
	v_mov_b32_e32 v55, v87
	v_pk_mov_b32 v[78:79], v[82:83], v[80:81] op_sel:[1,0]
	v_mov_b32_e32 v83, v81
	v_pk_add_f32 v[68:69], v[72:73], v[76:77]
	v_pk_add_f32 v[54:55], v[54:55], v[56:57]
	v_mul_f32_e32 v84, v51, v51
	v_mul_f32_e32 v86, v49, v49
	v_pk_add_f32 v[70:71], v[78:79], v[82:83]
	v_pk_add_f32 v[54:55], v[54:55], v[68:69]
	v_mul_f32_e32 v93, v52, v52
	v_mul_f32_e32 v94, v53, v53
	v_mul_f32_e32 v95, v46, v46
	v_mul_f32_e32 v96, v47, v47
	v_pk_fma_f32 v[80:81], v[50:51], v[50:51], v[84:85] op_sel_hi:[1,1,0]
	v_pk_fma_f32 v[84:85], v[48:49], v[48:49], v[86:87] op_sel_hi:[1,1,0]
	v_pk_add_f32 v[70:71], v[70:71], v[70:71] op_sel:[0,1] op_sel_hi:[1,0]
	v_pk_add_f32 v[54:55], v[54:55], v[54:55] op_sel:[0,1] op_sel_hi:[1,0]
	v_mov_b32_e32 v81, v95
	v_mov_b32_e32 v85, v96
	v_mov_b32_e32 v71, v94
	v_mov_b32_e32 v55, v93
	v_pk_add_f32 v[72:73], v[80:81], v[84:85]
	v_pk_add_f32 v[54:55], v[54:55], v[70:71]
	s_nop 0
	v_pk_add_f32 v[54:55], v[54:55], v[72:73]
	s_nop 0
	v_add_f32_e32 v54, v54, v55
	ds_bpermute_b32 v55, v58, v54
	s_waitcnt lgkmcnt(0)
; __device__ __forceinline__ void phase_final(const Ctx& P, volatile LAS int* tab, int vcu, int G) {
;     ...
;         ss = wave_sum(ss); const float rstd = __builtin_amdgcn_rsqf(ss * (1.0f / DM) + EPS);
; #pragma unroll
;         for (int j = 0; j < 8; ++j) { const int c = 4 * lane + 256 * j; const f32x4 fg = *(const f32x4*)(P.in[34] + c); *(f32x4*)(P.out + (size_t)row * DM + c) = v[j] * rstd * fg; }
;     }
	v_add_f32_e32 v54, v54, v55
	ds_bpermute_b32 v55, v59, v54
	s_waitcnt lgkmcnt(0)
	v_add_f32_e32 v54, v54, v55
	ds_bpermute_b32 v55, v60, v54
	s_waitcnt lgkmcnt(0)
	v_add_f32_e32 v54, v54, v55
	ds_bpermute_b32 v55, v61, v54
	s_waitcnt lgkmcnt(0)
	v_add_f32_e32 v54, v54, v55
	ds_bpermute_b32 v55, v62, v54
	s_waitcnt lgkmcnt(0)
	v_add_f32_e32 v54, v54, v55
	ds_bpermute_b32 v55, v63, v54
	s_waitcnt lgkmcnt(0)
	v_add_f32_e32 v54, v54, v55
	v_fmamk_f32 v54, v54, 0x3a000000, v67
	v_rsq_f32_e32 v54, v54
	s_nop 0
	v_pk_mul_f32 v[0:1], v[0:1], v[54:55] op_sel_hi:[1,0]
	v_pk_mul_f32 v[2:3], v[2:3], v[54:55] op_sel_hi:[1,0]
	v_pk_mul_f32 v[8:9], v[8:9], v[54:55] op_sel_hi:[1,0]
	v_pk_mul_f32 v[10:11], v[10:11], v[54:55] op_sel_hi:[1,0]
	v_pk_mul_f32 v[4:5], v[4:5], v[54:55] op_sel_hi:[1,0]
	v_pk_mul_f32 v[6:7], v[6:7], v[54:55] op_sel_hi:[1,0]
	v_pk_mul_f32 v[12:13], v[12:13], v[54:55] op_sel_hi:[1,0]
	v_pk_mul_f32 v[14:15], v[14:15], v[54:55] op_sel_hi:[1,0]
	v_pk_mul_f32 v[20:21], v[20:21], v[54:55] op_sel_hi:[1,0]
	v_pk_mul_f32 v[22:23], v[22:23], v[54:55] op_sel_hi:[1,0]
	v_pk_mul_f32 v[24:25], v[24:25], v[54:55] op_sel_hi:[1,0]
	v_pk_mul_f32 v[26:27], v[26:27], v[54:55] op_sel_hi:[1,0]
	v_pk_mul_f32 v[68:69], v[50:51], v[54:55] op_sel_hi:[1,0]
	v_pk_mul_f32 v[70:71], v[48:49], v[54:55] op_sel_hi:[1,0]
	v_pk_mul_f32 v[72:73], v[52:53], v[54:55] op_sel_hi:[1,0]
	v_pk_mul_f32 v[74:75], v[46:47], v[54:55] op_sel_hi:[1,0]
	v_pk_mul_f32 v[0:1], v[162:163], v[0:1]
	v_pk_mul_f32 v[2:3], v[164:165], v[2:3]
	global_store_dwordx4 v[32:33], v[0:3], off offset:-4096
	v_pk_mul_f32 v[8:9], v[166:167], v[8:9]
	v_pk_mul_f32 v[10:11], v[168:169], v[10:11]
	global_store_dwordx4 v[32:33], v[8:11], off offset:-3072
	v_pk_mul_f32 v[4:5], v[170:171], v[4:5]
	v_pk_mul_f32 v[6:7], v[172:173], v[6:7]
	global_store_dwordx4 v[32:33], v[4:7], off offset:-2048
	v_pk_mul_f32 v[12:13], v[174:175], v[12:13]
	v_pk_mul_f32 v[14:15], v[176:177], v[14:15]
	global_store_dwordx4 v[32:33], v[12:15], off offset:-1024
	v_pk_mul_f32 v[20:21], v[178:179], v[20:21]
	v_pk_mul_f32 v[22:23], v[180:181], v[22:23]
	global_store_dwordx4 v[32:33], v[20:23], off
	v_pk_mul_f32 v[24:25], v[182:183], v[24:25]
	v_pk_mul_f32 v[26:27], v[184:185], v[26:27]
	global_store_dwordx4 v[32:33], v[24:27], off offset:1024
	v_pk_mul_f32 v[68:69], v[186:187], v[68:69]
	v_pk_mul_f32 v[70:71], v[188:189], v[70:71]
	global_store_dwordx4 v[32:33], v[68:71], off offset:2048
	v_pk_mul_f32 v[72:73], v[190:191], v[72:73]
	v_pk_mul_f32 v[74:75], v[192:193], v[74:75]
	global_store_dwordx4 v[32:33], v[72:75], off offset:3072
	v_lshl_add_u64 v[32:33], v[32:33], 0, s[4:5]
	s_waitcnt vmcnt(8)
	s_cmp_eq_u32 s99, 2
	s_cbranch_scc0 .Lp16_nosleep
	s_sleep 127
	s_sleep 127
.Lp16_nosleep:
	s_cmp_lg_u32 s17, 0
	s_cbranch_scc1 .LBB0_2712
	s_branch .LBB0_2713
